# adds: GLA gate math reads the gla_low rows from LDS 3 reads ahead through a ring of 6 free register quads (was ~50 serial ds_read/lgkmcnt(0) round trips per unit)
# speedup vs baseline: 1.0079x; 1.0030x over previous
.LBB0_289:
	global_load_dword v199, v[2:3], off
	global_load_dword v198, v[2:3], off offset:2048
	s_lshl_b32 s8, s10, 4
	s_and_b32 s11, s8, 0xfffff800
	s_lshl_b32 s8, s10, 6
	s_ashr_i32 s18, s10, 5
	s_and_b32 s8, s8, 0x7c0
	s_lshl_b32 s14, s18, 7
	s_or_b32 s11, s11, s8
	s_and_b32 s33, s14, 0x180
	s_lshl_b32 s19, s33, 1
	v_readlane_b32 s14, v254, 38
	v_or_b32_e32 v2, s11, v1
	s_add_u32 s14, s14, s19
	v_readlane_b32 s15, v254, 40
	v_ashrrev_i32_e32 v3, 31, v2
	s_addc_u32 s15, s15, 0
	v_lshlrev_b64 v[2:3], 10, v[2:3]
	v_lshl_add_u64 v[226:227], s[14:15], 0, v[2:3]
	v_lshl_add_u64 v[226:227], v[226:227], 0, v[34:35]
	global_load_dwordx4 v[200:203], v[226:227], off
	v_readlane_b32 vcc_lo, v254, 42
	s_add_u32 vcc_lo, vcc_lo, s19
	v_readlane_b32 vcc_hi, v254, 44
	s_addc_u32 vcc_hi, vcc_hi, 0
	v_lshl_add_u64 v[228:229], vcc, 0, v[2:3]
	v_lshl_add_u64 v[228:229], v[228:229], 0, v[34:35]
	global_load_dwordx4 v[204:207], v[228:229], off
	v_or_b32_e32 v4, s11, v73
	v_ashrrev_i32_e32 v5, 31, v4
	v_lshlrev_b64 v[4:5], 10, v[4:5]
	v_lshl_add_u64 v[230:231], s[14:15], 0, v[4:5]
	v_lshl_add_u64 v[230:231], v[230:231], 0, v[34:35]
	global_load_dwordx4 v[218:221], v[230:231], off
	v_lshl_add_u64 v[232:233], vcc, 0, v[4:5]
	v_lshl_add_u64 v[232:233], v[232:233], 0, v[34:35]
	global_load_dwordx4 v[222:225], v[232:233], off
	s_movk_i32 s11, 0x1000
	v_readlane_b32 s14, v254, 58
	v_readlane_b32 s15, v254, 59
	v_or_b32_e32 v6, s33, v76
	v_lshlrev_b32_e32 v6, 2, v6
	v_mov_b32_e32 v7, v35
	v_lshl_add_u64 v[22:23], s[56:57], 0, v[6:7]
	v_add_co_u32_e32 v8, vcc, s11, v22
	s_movk_i32 s11, 0x2000
	s_nop 0
	v_addc_co_u32_e32 v9, vcc, 0, v23, vcc
	v_add_co_u32_e32 v10, vcc, s11, v22
	s_movk_i32 s11, 0x3000
	s_nop 0
	v_addc_co_u32_e32 v11, vcc, 0, v23, vcc
	global_load_dword v14, v6, s[56:57]
	global_load_dword v15, v6, s[56:57] offset:2048
	global_load_dword v16, v[10:11], off offset:-4096
	global_load_dword v17, v[8:9], off offset:2048
	global_load_dword v7, v[10:11], off
	s_nop 0
	global_load_dword v8, v[10:11], off offset:2048
	v_add_co_u32_e32 v10, vcc, s11, v22
	s_movk_i32 s11, 0x4000
	s_nop 0
	v_addc_co_u32_e32 v11, vcc, 0, v23, vcc
	v_add_co_u32_e32 v18, vcc, s11, v22
	s_movk_i32 s11, 0x5000
	s_nop 0
	v_addc_co_u32_e32 v19, vcc, 0, v23, vcc
	v_add_co_u32_e32 v20, vcc, s11, v22
	s_movk_i32 s11, 0x6000
	s_nop 0
	v_addc_co_u32_e32 v21, vcc, 0, v23, vcc
	v_add_co_u32_e32 v24, vcc, s11, v22
	s_movk_i32 s11, 0x7000
	s_nop 0
	v_addc_co_u32_e32 v25, vcc, 0, v23, vcc
	global_load_dword v12, v[18:19], off offset:-4096
	global_load_dword v13, v[10:11], off offset:2048
	global_load_dword v9, v[18:19], off
	s_nop 0
	global_load_dword v10, v[18:19], off offset:2048
	s_nop 0
	global_load_dword v19, v[24:25], off offset:-4096
	s_nop 0
	global_load_dword v20, v[20:21], off offset:2048
	s_nop 0
	global_load_dword v11, v[24:25], off
	global_load_dword v18, v[24:25], off offset:2048
	v_add_co_u32_e32 v24, vcc, s11, v22
	s_mov_b32 s11, 0xbd800000
	s_nop 0
	v_addc_co_u32_e32 v25, vcc, 0, v23, vcc
	global_load_dword v22, v[24:25], off
	global_load_dword v21, v[24:25], off offset:2048
	s_nop 0
	global_load_dword v24, v6, s[58:59]
	s_waitcnt vmcnt(22)
	ds_write_b32 v147, v199
	s_waitcnt vmcnt(21)
	ds_write_b32 v147, v198 offset:2048
	s_waitcnt vmcnt(20)
	ds_write_b128 v71, v[200:203] offset:59392
	s_waitcnt vmcnt(19)
	ds_write_b128 v72, v[204:207]
	s_waitcnt vmcnt(18)
	ds_write_b128 v74, v[218:221] offset:59392
	s_waitcnt vmcnt(17)
	ds_write_b128 v75, v[222:225]
	s_waitcnt lgkmcnt(0)
	s_barrier
	ds_read_b128 v[26:29], v77 offset:53248
	ds_read_b128 v[30:33], v77 offset:53264
	ds_read_b128 v[64:67], v77 offset:53280
	ds_read_b128 v[150:153], v77 offset:53296
	s_waitcnt vmcnt(15) lgkmcnt(3)
	v_mul_f32_e32 v6, v15, v27
	v_fmac_f32_e32 v6, v14, v26
	s_waitcnt vmcnt(11) lgkmcnt(2)
	v_mul_f32_e32 v23, v8, v31
	v_fmac_f32_e32 v6, v16, v28
	v_fmac_f32_e32 v23, v7, v30
	v_fmac_f32_e32 v6, v17, v29
	ds_read_b128 v[26:29], v77 offset:53312
	s_waitcnt vmcnt(10)
	v_fmac_f32_e32 v23, v12, v32
	s_waitcnt vmcnt(9)
	v_fmac_f32_e32 v23, v13, v33
	s_waitcnt vmcnt(0)
	v_add_f32_e32 v6, v24, v6
	v_add_f32_e32 v6, v6, v23
	s_waitcnt lgkmcnt(2)
	v_mul_f32_e32 v23, v10, v65
	v_fmac_f32_e32 v23, v9, v64
	v_fmac_f32_e32 v23, v19, v66
	v_fmac_f32_e32 v23, v20, v67
	v_add_f32_e32 v6, v6, v23
	s_waitcnt lgkmcnt(1)
	v_mul_f32_e32 v23, v18, v151
	v_fmac_f32_e32 v23, v11, v150
	v_fmac_f32_e32 v23, v22, v152
	v_fmac_f32_e32 v23, v21, v153
	v_add_f32_e32 v6, v6, v23
	v_mul_f32_e32 v6, 0x3fb8aa3b, v6
	v_max_f32_e64 v23, -v6, 0
	v_exp_f32_e64 v6, -|v6|
	ds_read_b128 v[64:67], v77 offset:53760
	ds_read_b128 v[150:153], v77 offset:54208
	v_add_f32_e32 v6, 1.0, v6
	v_log_f32_e32 v6, v6
	s_nop 0
	v_add_f32_e32 v6, v23, v6
	s_waitcnt lgkmcnt(2)
	v_mul_f32_e32 v23, v15, v27
	v_fmac_f32_e32 v23, v14, v26
	v_fmac_f32_e32 v23, v16, v28
	v_fmac_f32_e32 v23, v17, v29
	ds_read_b128 v[198:201], v77 offset:53328
	ds_read_b128 v[202:205], v77 offset:53344
	ds_read_b128 v[206:209], v77 offset:53360
	ds_read_b128 v[218:221], v77 offset:53376
	v_add_f32_e32 v23, v24, v23
	v_fma_f32 v6, v6, s11, 0
	s_waitcnt lgkmcnt(3)
	v_mul_f32_e32 v25, v8, v199
	v_fmac_f32_e32 v25, v7, v198
	v_fmac_f32_e32 v25, v12, v200
	v_fmac_f32_e32 v25, v13, v201
	ds_read_b128 v[222:225], v77 offset:53392
	v_add_f32_e32 v23, v23, v25
	s_waitcnt lgkmcnt(3)
	v_mul_f32_e32 v25, v10, v203
	v_fmac_f32_e32 v25, v9, v202
	v_fmac_f32_e32 v25, v19, v204
	v_fmac_f32_e32 v25, v20, v205
	ds_read_b128 v[226:229], v77 offset:53408
	v_add_f32_e32 v23, v23, v25
	s_waitcnt lgkmcnt(3)
	v_mul_f32_e32 v25, v18, v207
	v_fmac_f32_e32 v25, v11, v206
	v_fmac_f32_e32 v25, v22, v208
	v_fmac_f32_e32 v25, v21, v209
	v_add_f32_e32 v23, v23, v25
	v_mul_f32_e32 v23, 0x3fb8aa3b, v23
	v_max_f32_e64 v25, -v23, 0
	v_exp_f32_e64 v23, -|v23|
	ds_read_b128 v[198:201], v77 offset:53424
	v_add_f32_e32 v23, 1.0, v23
	v_log_f32_e32 v23, v23
	s_nop 0
	v_add_f32_e32 v23, v25, v23
	s_waitcnt lgkmcnt(3)
	v_mul_f32_e32 v25, v15, v219
	v_fmac_f32_e32 v25, v14, v218
	v_fmac_f32_e32 v25, v16, v220
	v_fmac_f32_e32 v25, v17, v221
	ds_read_b128 v[202:205], v77 offset:53440
	v_add_f32_e32 v25, v24, v25
	v_fmamk_f32 v23, v23, 0xbd800000, v6
	s_waitcnt lgkmcnt(3)
	v_mul_f32_e32 v27, v8, v223
	v_fmac_f32_e32 v27, v7, v222
	v_fmac_f32_e32 v27, v12, v224
	v_fmac_f32_e32 v27, v13, v225
	v_add_f32_e32 v25, v25, v27
	ds_read_b128 v[206:209], v77 offset:53456
	s_waitcnt lgkmcnt(3)
	v_mul_f32_e32 v27, v10, v227
	v_fmac_f32_e32 v27, v9, v226
	v_fmac_f32_e32 v27, v19, v228
	v_fmac_f32_e32 v27, v20, v229
	v_add_f32_e32 v25, v25, v27
	ds_read_b128 v[218:221], v77 offset:53472
	s_waitcnt lgkmcnt(3)
	v_mul_f32_e32 v27, v18, v199
	v_fmac_f32_e32 v27, v11, v198
	v_fmac_f32_e32 v27, v22, v200
	v_fmac_f32_e32 v27, v21, v201
	v_add_f32_e32 v25, v25, v27
	v_mul_f32_e32 v25, 0x3fb8aa3b, v25
	v_max_f32_e64 v26, -v25, 0
	v_exp_f32_e64 v25, -|v25|
	s_nop 0
	v_add_f32_e32 v25, 1.0, v25
	v_log_f32_e32 v25, v25
	s_nop 0
	v_add_f32_e32 v25, v26, v25
	ds_read_b128 v[222:225], v77 offset:53488
	v_fmamk_f32 v25, v25, 0xbd800000, v23
	s_waitcnt lgkmcnt(3)
	v_mul_f32_e32 v27, v15, v203
	v_fmac_f32_e32 v27, v14, v202
	v_fmac_f32_e32 v27, v16, v204
	v_fmac_f32_e32 v27, v17, v205
	v_add_f32_e32 v30, v24, v27
	ds_read_b128 v[226:229], v77 offset:53504
	s_waitcnt lgkmcnt(3)
	v_mul_f32_e32 v27, v8, v207
	v_fmac_f32_e32 v27, v7, v206
	v_fmac_f32_e32 v27, v12, v208
	v_fmac_f32_e32 v27, v13, v209
	v_add_f32_e32 v30, v30, v27
	ds_read_b128 v[198:201], v77 offset:53520
	s_waitcnt lgkmcnt(3)
	v_mul_f32_e32 v27, v10, v219
	v_fmac_f32_e32 v27, v9, v218
	v_fmac_f32_e32 v27, v19, v220
	v_fmac_f32_e32 v27, v20, v221
	v_add_f32_e32 v30, v30, v27
	ds_read_b128 v[202:205], v77 offset:53536
	s_waitcnt lgkmcnt(3)
	v_mul_f32_e32 v27, v18, v223
	v_fmac_f32_e32 v27, v11, v222
	v_fmac_f32_e32 v27, v22, v224
	v_fmac_f32_e32 v27, v21, v225
	v_add_f32_e32 v26, v30, v27
	v_mul_f32_e32 v26, 0x3fb8aa3b, v26
	v_max_f32_e64 v27, -v26, 0
	v_exp_f32_e64 v26, -|v26|
	ds_read_b128 v[206:209], v77 offset:53552
	v_add_f32_e32 v26, 1.0, v26
	v_log_f32_e32 v26, v26
	s_nop 0
	v_add_f32_e32 v26, v27, v26
	s_waitcnt lgkmcnt(3)
	v_mul_f32_e32 v27, v15, v227
	v_fmac_f32_e32 v27, v14, v226
	v_fmac_f32_e32 v27, v16, v228
	v_fmac_f32_e32 v27, v17, v229
	ds_read_b128 v[218:221], v77 offset:53568
	v_add_f32_e32 v27, v24, v27
	v_fmamk_f32 v26, v26, 0xbd800000, v25
	s_waitcnt lgkmcnt(3)
	v_mul_f32_e32 v29, v8, v199
	v_fmac_f32_e32 v29, v7, v198
	v_fmac_f32_e32 v29, v12, v200
	v_fmac_f32_e32 v29, v13, v201
	v_add_f32_e32 v27, v27, v29
	ds_read_b128 v[222:225], v77 offset:53584
	s_waitcnt lgkmcnt(3)
	v_mul_f32_e32 v29, v10, v203
	v_fmac_f32_e32 v29, v9, v202
	v_fmac_f32_e32 v29, v19, v204
	v_fmac_f32_e32 v29, v20, v205
	v_add_f32_e32 v27, v27, v29
	ds_read_b128 v[226:229], v77 offset:53600
	s_waitcnt lgkmcnt(3)
	v_mul_f32_e32 v29, v18, v207
	v_fmac_f32_e32 v29, v11, v206
	v_fmac_f32_e32 v29, v22, v208
	v_fmac_f32_e32 v29, v21, v209
	v_add_f32_e32 v27, v27, v29
	v_mul_f32_e32 v27, 0x3fb8aa3b, v27
	v_max_f32_e64 v28, -v27, 0
	v_exp_f32_e64 v27, -|v27|
	s_nop 0
	v_add_f32_e32 v27, 1.0, v27
	v_log_f32_e32 v27, v27
	s_nop 0
	v_add_f32_e32 v27, v28, v27
	ds_read_b128 v[198:201], v77 offset:53616
	v_fmamk_f32 v27, v27, 0xbd800000, v26
	s_waitcnt lgkmcnt(3)
	v_mul_f32_e32 v29, v15, v219
	v_fmac_f32_e32 v29, v14, v218
	v_fmac_f32_e32 v29, v16, v220
	v_fmac_f32_e32 v29, v17, v221
	v_add_f32_e32 v32, v24, v29
	ds_read_b128 v[202:205], v77 offset:53632
	s_waitcnt lgkmcnt(3)
	v_mul_f32_e32 v29, v8, v223
	v_fmac_f32_e32 v29, v7, v222
	v_fmac_f32_e32 v29, v12, v224
	v_fmac_f32_e32 v29, v13, v225
	v_add_f32_e32 v32, v32, v29
	ds_read_b128 v[206:209], v77 offset:53648
	s_waitcnt lgkmcnt(3)
	v_mul_f32_e32 v29, v10, v227
	v_fmac_f32_e32 v29, v9, v226
	v_fmac_f32_e32 v29, v19, v228
	v_fmac_f32_e32 v29, v20, v229
	v_add_f32_e32 v32, v32, v29
	ds_read_b128 v[218:221], v77 offset:53664
	s_waitcnt lgkmcnt(3)
	v_mul_f32_e32 v29, v18, v199
	v_fmac_f32_e32 v29, v11, v198
	v_fmac_f32_e32 v29, v22, v200
	v_fmac_f32_e32 v29, v21, v201
	v_add_f32_e32 v28, v32, v29
	v_mul_f32_e32 v28, 0x3fb8aa3b, v28
	v_max_f32_e64 v29, -v28, 0
	v_exp_f32_e64 v28, -|v28|
	ds_read_b128 v[222:225], v77 offset:53680
	v_add_f32_e32 v28, 1.0, v28
	v_log_f32_e32 v28, v28
	s_nop 0
	v_add_f32_e32 v28, v29, v28
	s_waitcnt lgkmcnt(3)
	v_mul_f32_e32 v29, v15, v203
	v_fmac_f32_e32 v29, v14, v202
	v_fmac_f32_e32 v29, v16, v204
	v_fmac_f32_e32 v29, v17, v205
	ds_read_b128 v[226:229], v77 offset:53696
	v_add_f32_e32 v29, v24, v29
	v_fmamk_f32 v28, v28, 0xbd800000, v27
	s_waitcnt lgkmcnt(3)
	v_mul_f32_e32 v31, v8, v207
	v_fmac_f32_e32 v31, v7, v206
	v_fmac_f32_e32 v31, v12, v208
	v_fmac_f32_e32 v31, v13, v209
	v_add_f32_e32 v29, v29, v31
	ds_read_b128 v[198:201], v77 offset:53712
	s_waitcnt lgkmcnt(3)
	v_mul_f32_e32 v31, v10, v219
	v_fmac_f32_e32 v31, v9, v218
	v_fmac_f32_e32 v31, v19, v220
	v_fmac_f32_e32 v31, v20, v221
	v_add_f32_e32 v29, v29, v31
	ds_read_b128 v[202:205], v77 offset:53728
	s_waitcnt lgkmcnt(3)
	v_mul_f32_e32 v31, v18, v223
	v_fmac_f32_e32 v31, v11, v222
	v_fmac_f32_e32 v31, v22, v224
	v_fmac_f32_e32 v31, v21, v225
	v_add_f32_e32 v29, v29, v31
	v_mul_f32_e32 v29, 0x3fb8aa3b, v29
	v_max_f32_e64 v30, -v29, 0
	v_exp_f32_e64 v29, -|v29|
	s_nop 0
	v_add_f32_e32 v29, 1.0, v29
	v_log_f32_e32 v29, v29
	s_nop 0
	v_add_f32_e32 v29, v30, v29
	ds_read_b128 v[206:209], v77 offset:53744
	v_fmamk_f32 v29, v29, 0xbd800000, v28
	s_waitcnt lgkmcnt(3)
	v_mul_f32_e32 v31, v15, v227
	v_fmac_f32_e32 v31, v14, v226
	v_fmac_f32_e32 v31, v16, v228
	v_fmac_f32_e32 v31, v17, v229
	v_add_f32_e32 v63, v24, v31
	ds_read_b128 v[218:221], v77 offset:53776
	s_waitcnt lgkmcnt(3)
	v_mul_f32_e32 v31, v8, v199
	v_fmac_f32_e32 v31, v7, v198
	v_fmac_f32_e32 v31, v12, v200
	v_fmac_f32_e32 v31, v13, v201
	v_add_f32_e32 v63, v63, v31
	ds_read_b128 v[222:225], v77 offset:53792
	s_waitcnt lgkmcnt(3)
	v_mul_f32_e32 v31, v10, v203
	v_fmac_f32_e32 v31, v9, v202
	v_fmac_f32_e32 v31, v19, v204
	v_fmac_f32_e32 v31, v20, v205
	v_add_f32_e32 v63, v63, v31
	ds_read_b128 v[226:229], v77 offset:53808
	s_waitcnt lgkmcnt(3)
	v_mul_f32_e32 v31, v18, v207
	v_fmac_f32_e32 v31, v11, v206
	v_fmac_f32_e32 v31, v22, v208
	v_fmac_f32_e32 v31, v21, v209
	v_add_f32_e32 v30, v63, v31
	v_mul_f32_e32 v30, 0x3fb8aa3b, v30
	v_max_f32_e64 v31, -v30, 0
	v_exp_f32_e64 v30, -|v30|
	s_nop 0
	v_add_f32_e32 v30, 1.0, v30
	v_log_f32_e32 v30, v30
	s_nop 0
	v_add_f32_e32 v30, v31, v30
	v_mul_f32_e32 v31, v15, v65
	v_fmac_f32_e32 v31, v14, v64
	v_fmac_f32_e32 v31, v16, v66
	v_fmac_f32_e32 v31, v17, v67
	ds_read_b128 v[198:201], v77 offset:53824
	v_add_f32_e32 v31, v24, v31
	v_fmamk_f32 v30, v30, 0xbd800000, v29
	s_waitcnt lgkmcnt(3)
	v_mul_f32_e32 v32, v8, v219
	v_fmac_f32_e32 v32, v7, v218
	v_fmac_f32_e32 v32, v12, v220
	v_fmac_f32_e32 v32, v13, v221
	ds_read_b128 v[202:205], v77 offset:53840
	v_add_f32_e32 v31, v31, v32
	s_waitcnt lgkmcnt(3)
	v_mul_f32_e32 v32, v10, v223
	v_fmac_f32_e32 v32, v9, v222
	v_fmac_f32_e32 v32, v19, v224
	v_fmac_f32_e32 v32, v20, v225
	ds_read_b128 v[206:209], v77 offset:53856
	v_add_f32_e32 v31, v31, v32
	s_waitcnt lgkmcnt(3)
	v_mul_f32_e32 v32, v18, v227
	v_fmac_f32_e32 v32, v11, v226
	v_fmac_f32_e32 v32, v22, v228
	v_fmac_f32_e32 v32, v21, v229
	v_add_f32_e32 v31, v31, v32
	v_mul_f32_e32 v31, 0x3fb8aa3b, v31
	v_max_f32_e64 v32, -v31, 0
	v_exp_f32_e64 v31, -|v31|
	ds_read_b128 v[218:221], v77 offset:53872
	v_add_f32_e32 v31, 1.0, v31
	v_log_f32_e32 v31, v31
	s_nop 0
	v_add_f32_e32 v31, v32, v31
	s_waitcnt lgkmcnt(3)
	v_mul_f32_e32 v32, v15, v199
	v_fmac_f32_e32 v32, v14, v198
	v_fmac_f32_e32 v32, v16, v200
	v_fmac_f32_e32 v32, v17, v201
	ds_read_b128 v[222:225], v77 offset:53888
	v_add_f32_e32 v32, v24, v32
	v_fmamk_f32 v31, v31, 0xbd800000, v30
	s_waitcnt lgkmcnt(3)
	v_mul_f32_e32 v33, v8, v203
	v_fmac_f32_e32 v33, v7, v202
	v_fmac_f32_e32 v33, v12, v204
	v_fmac_f32_e32 v33, v13, v205
	ds_read_b128 v[226:229], v77 offset:53904
	v_add_f32_e32 v32, v32, v33
	s_waitcnt lgkmcnt(3)
	v_mul_f32_e32 v33, v10, v207
	v_fmac_f32_e32 v33, v9, v206
	v_fmac_f32_e32 v33, v19, v208
	v_fmac_f32_e32 v33, v20, v209
	ds_read_b128 v[198:201], v77 offset:53920
	v_add_f32_e32 v32, v32, v33
	s_waitcnt lgkmcnt(3)
	v_mul_f32_e32 v33, v18, v219
	v_fmac_f32_e32 v33, v11, v218
	v_fmac_f32_e32 v33, v22, v220
	v_fmac_f32_e32 v33, v21, v221
	v_add_f32_e32 v32, v32, v33
	v_mul_f32_e32 v32, 0x3fb8aa3b, v32
	v_max_f32_e64 v33, -v32, 0
	v_exp_f32_e64 v32, -|v32|
	ds_read_b128 v[202:205], v77 offset:53936
	v_add_f32_e32 v32, 1.0, v32
	v_log_f32_e32 v32, v32
	s_nop 0
	v_add_f32_e32 v32, v33, v32
	s_waitcnt lgkmcnt(3)
	v_mul_f32_e32 v33, v15, v223
	v_fmac_f32_e32 v33, v14, v222
	v_fmac_f32_e32 v33, v16, v224
	v_fmac_f32_e32 v33, v17, v225
	ds_read_b128 v[206:209], v77 offset:53952
	v_add_f32_e32 v33, v24, v33
	v_fmamk_f32 v32, v32, 0xbd800000, v31
	s_waitcnt lgkmcnt(3)
	v_mul_f32_e32 v63, v8, v227
	v_fmac_f32_e32 v63, v7, v226
	v_fmac_f32_e32 v63, v12, v228
	v_fmac_f32_e32 v63, v13, v229
	ds_read_b128 v[218:221], v77 offset:53968
	v_add_f32_e32 v33, v33, v63
	s_waitcnt lgkmcnt(3)
	v_mul_f32_e32 v63, v10, v199
	v_fmac_f32_e32 v63, v9, v198
	v_fmac_f32_e32 v63, v19, v200
	v_fmac_f32_e32 v63, v20, v201
	ds_read_b128 v[222:225], v77 offset:53984
	v_add_f32_e32 v33, v33, v63
	s_waitcnt lgkmcnt(3)
	v_mul_f32_e32 v63, v18, v203
	v_fmac_f32_e32 v63, v11, v202
	v_fmac_f32_e32 v63, v22, v204
	v_fmac_f32_e32 v63, v21, v205
	v_add_f32_e32 v33, v33, v63
	v_mul_f32_e32 v33, 0x3fb8aa3b, v33
	v_max_f32_e64 v63, -v33, 0
	v_exp_f32_e64 v33, -|v33|
	ds_read_b128 v[226:229], v77 offset:54000
	v_add_f32_e32 v33, 1.0, v33
	v_log_f32_e32 v33, v33
	s_nop 0
	v_add_f32_e32 v33, v63, v33
	s_waitcnt lgkmcnt(3)
	v_mul_f32_e32 v63, v15, v207
	v_fmac_f32_e32 v63, v14, v206
	v_fmac_f32_e32 v63, v16, v208
	v_fmac_f32_e32 v63, v17, v209
	ds_read_b128 v[198:201], v77 offset:54016
	v_add_f32_e32 v63, v24, v63
	v_fmamk_f32 v33, v33, 0xbd800000, v32
	s_waitcnt lgkmcnt(3)
	v_mul_f32_e32 v65, v8, v219
	v_fmac_f32_e32 v65, v7, v218
	v_fmac_f32_e32 v65, v12, v220
	v_fmac_f32_e32 v65, v13, v221
	v_add_f32_e32 v63, v63, v65
	ds_read_b128 v[202:205], v77 offset:54032
	s_waitcnt lgkmcnt(3)
	v_mul_f32_e32 v65, v10, v223
	v_fmac_f32_e32 v65, v9, v222
	v_fmac_f32_e32 v65, v19, v224
	v_fmac_f32_e32 v65, v20, v225
	v_add_f32_e32 v63, v63, v65
	ds_read_b128 v[206:209], v77 offset:54048
	s_waitcnt lgkmcnt(3)
	v_mul_f32_e32 v65, v18, v227
	v_fmac_f32_e32 v65, v11, v226
	v_fmac_f32_e32 v65, v22, v228
	v_fmac_f32_e32 v65, v21, v229
	v_add_f32_e32 v63, v63, v65
	v_mul_f32_e32 v63, 0x3fb8aa3b, v63
	v_max_f32_e64 v64, -v63, 0
	v_exp_f32_e64 v63, -|v63|
	s_nop 0
	v_add_f32_e32 v63, 1.0, v63
	v_log_f32_e32 v63, v63
	s_nop 0
	v_add_f32_e32 v63, v64, v63
	ds_read_b128 v[218:221], v77 offset:54064
	v_fmamk_f32 v63, v63, 0xbd800000, v33
	s_waitcnt lgkmcnt(3)
	v_mul_f32_e32 v65, v15, v199
	v_fmac_f32_e32 v65, v14, v198
	v_fmac_f32_e32 v65, v16, v200
	v_fmac_f32_e32 v65, v17, v201
	v_add_f32_e32 v68, v24, v65
	ds_read_b128 v[222:225], v77 offset:54080
	s_waitcnt lgkmcnt(3)
	v_mul_f32_e32 v65, v8, v203
	v_fmac_f32_e32 v65, v7, v202
	v_fmac_f32_e32 v65, v12, v204
	v_fmac_f32_e32 v65, v13, v205
	v_add_f32_e32 v68, v68, v65
	ds_read_b128 v[226:229], v77 offset:54096
	s_waitcnt lgkmcnt(3)
	v_mul_f32_e32 v65, v10, v207
	v_fmac_f32_e32 v65, v9, v206
	v_fmac_f32_e32 v65, v19, v208
	v_fmac_f32_e32 v65, v20, v209
	v_add_f32_e32 v68, v68, v65
	ds_read_b128 v[198:201], v77 offset:54112
	s_waitcnt lgkmcnt(3)
	v_mul_f32_e32 v65, v18, v219
	v_fmac_f32_e32 v65, v11, v218
	v_fmac_f32_e32 v65, v22, v220
	v_fmac_f32_e32 v65, v21, v221
	v_add_f32_e32 v64, v68, v65
	v_mul_f32_e32 v64, 0x3fb8aa3b, v64
	v_max_f32_e64 v65, -v64, 0
	v_exp_f32_e64 v64, -|v64|
	ds_read_b128 v[202:205], v77 offset:54128
	v_add_f32_e32 v64, 1.0, v64
	v_log_f32_e32 v64, v64
	s_nop 0
	v_add_f32_e32 v64, v65, v64
	s_waitcnt lgkmcnt(3)
	v_mul_f32_e32 v65, v15, v223
	v_fmac_f32_e32 v65, v14, v222
	v_fmac_f32_e32 v65, v16, v224
	v_fmac_f32_e32 v65, v17, v225
	ds_read_b128 v[206:209], v77 offset:54144
	v_add_f32_e32 v65, v24, v65
	v_fmamk_f32 v64, v64, 0xbd800000, v63
	s_waitcnt lgkmcnt(3)
	v_mul_f32_e32 v67, v8, v227
	v_fmac_f32_e32 v67, v7, v226
	v_fmac_f32_e32 v67, v12, v228
	v_fmac_f32_e32 v67, v13, v229
	v_add_f32_e32 v65, v65, v67
	s_waitcnt lgkmcnt(2)
	v_mul_f32_e32 v67, v10, v199
	v_fmac_f32_e32 v67, v9, v198
	v_fmac_f32_e32 v67, v19, v200
	v_fmac_f32_e32 v67, v20, v201
	v_add_f32_e32 v65, v65, v67
	s_waitcnt lgkmcnt(1)
	v_mul_f32_e32 v67, v18, v203
	v_fmac_f32_e32 v67, v11, v202
	v_fmac_f32_e32 v67, v22, v204
	v_fmac_f32_e32 v67, v21, v205
	v_add_f32_e32 v65, v65, v67
	v_mul_f32_e32 v65, 0x3fb8aa3b, v65
	v_max_f32_e64 v66, -v65, 0
	v_exp_f32_e64 v65, -|v65|
	s_nop 0
	v_add_f32_e32 v65, 1.0, v65
	v_log_f32_e32 v65, v65
	s_nop 0
	v_add_f32_e32 v65, v66, v65
	v_fmamk_f32 v65, v65, 0xbd800000, v64
	s_waitcnt lgkmcnt(0)
	v_mul_f32_e32 v67, v15, v207
	v_fmac_f32_e32 v67, v14, v206
	v_fmac_f32_e32 v67, v16, v208
	v_fmac_f32_e32 v67, v17, v209
	v_mul_f32_e32 v15, v15, v151
	v_add_f32_e32 v149, v24, v67
	v_mov_b32_e32 v66, v206
	v_mov_b32_e32 v68, v208
	v_mov_b32_e32 v69, v209
	ds_read_b128 v[66:69], v77 offset:54160
	v_fmac_f32_e32 v15, v14, v150
	v_fmac_f32_e32 v15, v16, v152
	v_fmac_f32_e32 v15, v17, v153
	v_add_f32_e32 v24, v24, v15
	ds_read_b128 v[14:17], v77 offset:54224
	s_waitcnt lgkmcnt(1)
	v_mul_f32_e32 v67, v8, v67
	v_fmac_f32_e32 v67, v7, v66
	v_fmac_f32_e32 v67, v12, v68
	v_fmac_f32_e32 v67, v13, v69
	s_waitcnt lgkmcnt(0)
	v_mul_f32_e32 v8, v8, v15
	v_add_f32_e32 v149, v149, v67
	ds_read_b128 v[66:69], v77 offset:54176
	v_fmac_f32_e32 v8, v7, v14
	v_fmac_f32_e32 v8, v12, v16
	v_fmac_f32_e32 v8, v13, v17
	ds_read_b128 v[12:15], v77 offset:54240
	s_waitcnt lgkmcnt(1)
	v_mul_f32_e32 v67, v10, v67
	v_fmac_f32_e32 v67, v9, v66
	v_fmac_f32_e32 v67, v19, v68
	v_add_f32_e32 v7, v24, v8
	s_waitcnt lgkmcnt(0)
	v_mul_f32_e32 v8, v10, v13
	v_fmac_f32_e32 v67, v20, v69
	v_fmac_f32_e32 v8, v9, v12
	v_add_f32_e32 v149, v149, v67
	ds_read_b128 v[66:69], v77 offset:54192
	v_fmac_f32_e32 v8, v19, v14
	v_fmac_f32_e32 v8, v20, v15
	ds_read_b128 v[12:15], v77 offset:54256
	v_add_f32_e32 v7, v7, v8
	s_waitcnt lgkmcnt(1)
	v_mul_f32_e32 v67, v18, v67
	v_fmac_f32_e32 v67, v11, v66
	v_fmac_f32_e32 v67, v22, v68
	s_waitcnt lgkmcnt(0)
	v_mul_f32_e32 v8, v18, v13
	v_fmac_f32_e32 v8, v11, v12
	v_fmac_f32_e32 v67, v21, v69
	v_fmac_f32_e32 v8, v22, v14
	v_add_f32_e32 v66, v149, v67
	v_fmac_f32_e32 v8, v21, v15
	v_mul_f32_e32 v66, 0x3fb8aa3b, v66
	v_add_f32_e32 v7, v7, v8
	v_max_f32_e64 v67, -v66, 0
	v_exp_f32_e64 v66, -|v66|
	v_mul_f32_e32 v7, 0x3fb8aa3b, v7
	v_max_f32_e64 v8, -v7, 0
	v_exp_f32_e64 v7, -|v7|
	v_add_f32_e32 v66, 1.0, v66
	v_log_f32_e32 v66, v66
	v_add_f32_e32 v7, 1.0, v7
	v_log_f32_e32 v7, v7
	v_add_f32_e32 v66, v67, v66
	v_fmamk_f32 v66, v66, 0xbd800000, v65
	v_add_f32_e32 v7, v8, v7
	v_fmamk_f32 v8, v7, 0xbd800000, v66
	ds_write_b32 v78, v8 offset:57344
	s_waitcnt lgkmcnt(0)
	s_barrier
	ds_read2st64_b32 v[10:11], v79 offset0:224 offset1:226
	s_waitcnt lgkmcnt(0)
	v_add_f32_e32 v7, 0, v10
	v_cndmask_b32_e64 v9, v7, 0, s[14:15]
	v_readlane_b32 s14, v254, 62
	v_add_f32_e32 v10, v11, v9
	v_readlane_b32 s15, v254, 63
	v_add_f32_e32 v7, v7, v11
	s_nop 0
	v_cndmask_b32_e64 v9, v9, v10, s[14:15]
	ds_read2st64_b32 v[10:11], v79 offset0:228 offset1:230
	v_readlane_b32 s14, v255, 0
	v_readlane_b32 s15, v255, 1
	s_waitcnt lgkmcnt(0)
	v_add_f32_e32 v7, v7, v10
	v_add_f32_e32 v10, v10, v9
	v_cndmask_b32_e64 v9, v9, v10, s[14:15]
	v_readlane_b32 s14, v255, 2
	v_add_f32_e32 v10, v11, v9
	v_readlane_b32 s15, v255, 3
	v_add_f32_e32 v7, v7, v11
	ds_read_u16 v11, v81
	v_cndmask_b32_e64 v9, v9, v10, s[14:15]
	ds_read_u16 v10, v80 offset:59392
	v_add_f32_e32 v6, v6, v9
	v_exp_f32_e32 v12, v6
	s_waitcnt lgkmcnt(1)
	v_lshlrev_b32_e32 v11, 16, v11
	s_waitcnt lgkmcnt(0)
	v_lshlrev_b32_e32 v10, 16, v10
	v_mul_f32_e32 v10, 0x3db504f3, v10
	v_mul_f32_e32 v10, v10, v12
	v_cvt_pk_bf16_f32 v10, v10, s0
	ds_write_b16 v82, v10
	v_exp_f32_e64 v10, -v6
	v_sub_f32_e32 v6, v7, v6
	v_exp_f32_e32 v6, v6
	v_mul_f32_e32 v10, v10, v11
	v_cvt_pk_bf16_f32 v10, v10, s0
	v_mul_f32_e32 v6, v6, v11
	v_cvt_pk_bf16_f32 v6, v6, s0
	ds_write_b16 v82, v10 offset:17408
	ds_write_b16 v83, v6 offset:34816
	ds_read_u16 v10, v84 offset:59392
	ds_read_u16 v11, v85
	v_add_f32_e32 v6, v23, v9
	v_exp_f32_e32 v12, v6
	s_waitcnt lgkmcnt(1)
	v_lshlrev_b32_e32 v10, 16, v10
	v_mul_f32_e32 v10, 0x3db504f3, v10
	v_mul_f32_e32 v10, v12, v10
	v_cvt_pk_bf16_f32 v10, v10, s0
	ds_write_b16 v86, v10
	v_exp_f32_e64 v10, -v6
	v_sub_f32_e32 v6, v7, v6
	v_exp_f32_e32 v6, v6
	s_waitcnt lgkmcnt(1)
	v_lshlrev_b32_e32 v11, 16, v11
	v_mul_f32_e32 v10, v10, v11
	v_cvt_pk_bf16_f32 v10, v10, s0
	v_mul_f32_e32 v6, v6, v11
	v_cvt_pk_bf16_f32 v6, v6, s0
	ds_write_b16 v86, v10 offset:17408
	ds_write_b16 v83, v6 offset:34818
	ds_read_u16 v10, v87 offset:59392
	ds_read_u16 v11, v88
	v_add_f32_e32 v6, v25, v9
	v_exp_f32_e32 v12, v6
	s_waitcnt lgkmcnt(1)
	v_lshlrev_b32_e32 v10, 16, v10
	v_mul_f32_e32 v10, 0x3db504f3, v10
	v_mul_f32_e32 v10, v12, v10
	v_cvt_pk_bf16_f32 v10, v10, s0
	ds_write_b16 v89, v10
	v_exp_f32_e64 v10, -v6
	v_sub_f32_e32 v6, v7, v6
	v_exp_f32_e32 v6, v6
	s_waitcnt lgkmcnt(1)
	v_lshlrev_b32_e32 v11, 16, v11
	v_mul_f32_e32 v10, v10, v11
	v_cvt_pk_bf16_f32 v10, v10, s0
	v_mul_f32_e32 v6, v6, v11
	v_cvt_pk_bf16_f32 v6, v6, s0
	ds_write_b16 v89, v10 offset:17408
	ds_write_b16 v83, v6 offset:34820
	ds_read_u16 v10, v90 offset:59392
	ds_read_u16 v11, v91
	v_add_f32_e32 v6, v26, v9
	v_exp_f32_e32 v12, v6
	s_waitcnt lgkmcnt(1)
	v_lshlrev_b32_e32 v10, 16, v10
	v_mul_f32_e32 v10, 0x3db504f3, v10
	v_mul_f32_e32 v10, v12, v10
	v_cvt_pk_bf16_f32 v10, v10, s0
	ds_write_b16 v92, v10
	v_exp_f32_e64 v10, -v6
	v_sub_f32_e32 v6, v7, v6
	v_exp_f32_e32 v6, v6
	s_waitcnt lgkmcnt(1)
	v_lshlrev_b32_e32 v11, 16, v11
	v_mul_f32_e32 v10, v10, v11
	v_cvt_pk_bf16_f32 v10, v10, s0
	v_mul_f32_e32 v6, v6, v11
	v_cvt_pk_bf16_f32 v6, v6, s0
	ds_write_b16 v92, v10 offset:17408
	ds_write_b16 v83, v6 offset:34822
	ds_read_u16 v10, v93 offset:59392
	ds_read_u16 v11, v94
	v_add_f32_e32 v6, v27, v9
	v_exp_f32_e32 v12, v6
	s_waitcnt lgkmcnt(1)
	v_lshlrev_b32_e32 v10, 16, v10
	v_mul_f32_e32 v10, 0x3db504f3, v10
	v_mul_f32_e32 v10, v12, v10
	v_cvt_pk_bf16_f32 v10, v10, s0
	ds_write_b16 v95, v10
	v_exp_f32_e64 v10, -v6
	v_sub_f32_e32 v6, v7, v6
	v_exp_f32_e32 v6, v6
	s_waitcnt lgkmcnt(1)
	v_lshlrev_b32_e32 v11, 16, v11
	v_mul_f32_e32 v10, v10, v11
	v_cvt_pk_bf16_f32 v10, v10, s0
	v_mul_f32_e32 v6, v6, v11
	v_cvt_pk_bf16_f32 v6, v6, s0
	ds_write_b16 v95, v10 offset:17408
	ds_write_b16 v83, v6 offset:34824
	ds_read_u16 v10, v96 offset:59392
	ds_read_u16 v11, v97
	v_add_f32_e32 v6, v28, v9
	v_exp_f32_e32 v12, v6
	s_waitcnt lgkmcnt(1)
	v_lshlrev_b32_e32 v10, 16, v10
	v_mul_f32_e32 v10, 0x3db504f3, v10
	v_mul_f32_e32 v10, v12, v10
	v_cvt_pk_bf16_f32 v10, v10, s0
	ds_write_b16 v98, v10
	v_exp_f32_e64 v10, -v6
	v_sub_f32_e32 v6, v7, v6
	v_exp_f32_e32 v6, v6
	s_waitcnt lgkmcnt(1)
	v_lshlrev_b32_e32 v11, 16, v11
	v_mul_f32_e32 v10, v10, v11
	v_cvt_pk_bf16_f32 v10, v10, s0
	v_mul_f32_e32 v6, v6, v11
	v_cvt_pk_bf16_f32 v6, v6, s0
	ds_write_b16 v98, v10 offset:17408
	ds_write_b16 v83, v6 offset:34826
	ds_read_u16 v10, v99 offset:59392
	ds_read_u16 v11, v100
	v_add_f32_e32 v6, v29, v9
	v_exp_f32_e32 v12, v6
	s_waitcnt lgkmcnt(1)
	v_lshlrev_b32_e32 v10, 16, v10
	v_mul_f32_e32 v10, 0x3db504f3, v10
	v_mul_f32_e32 v10, v12, v10
	v_cvt_pk_bf16_f32 v10, v10, s0
	ds_write_b16 v101, v10
	v_exp_f32_e64 v10, -v6
	v_sub_f32_e32 v6, v7, v6
	v_exp_f32_e32 v6, v6
	s_waitcnt lgkmcnt(1)
	v_lshlrev_b32_e32 v11, 16, v11
	v_mul_f32_e32 v10, v10, v11
	v_cvt_pk_bf16_f32 v10, v10, s0
	v_mul_f32_e32 v6, v6, v11
	v_cvt_pk_bf16_f32 v6, v6, s0
	ds_write_b16 v101, v10 offset:17408
	ds_write_b16 v83, v6 offset:34828
	ds_read_u16 v10, v102 offset:59392
	ds_read_u16 v11, v103
	v_add_f32_e32 v6, v30, v9
	v_exp_f32_e32 v12, v6
	s_waitcnt lgkmcnt(1)
	v_lshlrev_b32_e32 v10, 16, v10
	v_mul_f32_e32 v10, 0x3db504f3, v10
	v_mul_f32_e32 v10, v12, v10
	v_cvt_pk_bf16_f32 v10, v10, s0
	ds_write_b16 v104, v10
	v_exp_f32_e64 v10, -v6
	v_sub_f32_e32 v6, v7, v6
	v_exp_f32_e32 v6, v6
	s_waitcnt lgkmcnt(1)
	v_lshlrev_b32_e32 v11, 16, v11
	v_mul_f32_e32 v10, v10, v11
	v_cvt_pk_bf16_f32 v10, v10, s0
	v_mul_f32_e32 v6, v6, v11
	v_cvt_pk_bf16_f32 v6, v6, s0
	ds_write_b16 v104, v10 offset:17408
	ds_write_b16 v83, v6 offset:34830
	ds_read_u16 v10, v105 offset:59392
	ds_read_u16 v11, v106
	v_add_f32_e32 v6, v31, v9
	v_exp_f32_e32 v12, v6
	s_waitcnt lgkmcnt(1)
	v_lshlrev_b32_e32 v10, 16, v10
	v_mul_f32_e32 v10, 0x3db504f3, v10
	v_mul_f32_e32 v10, v12, v10
	v_cvt_pk_bf16_f32 v10, v10, s0
	ds_write_b16 v107, v10
	v_exp_f32_e64 v10, -v6
	v_sub_f32_e32 v6, v7, v6
	v_exp_f32_e32 v6, v6
	s_waitcnt lgkmcnt(1)
	v_lshlrev_b32_e32 v11, 16, v11
	v_mul_f32_e32 v10, v10, v11
	v_cvt_pk_bf16_f32 v10, v10, s0
	v_mul_f32_e32 v6, v6, v11
	v_cvt_pk_bf16_f32 v6, v6, s0
	ds_write_b16 v107, v10 offset:17408
	ds_write_b16 v83, v6 offset:34832
	ds_read_u16 v10, v108 offset:59392
	ds_read_u16 v11, v109
	v_add_f32_e32 v6, v32, v9
	v_exp_f32_e32 v12, v6
	s_waitcnt lgkmcnt(1)
	v_lshlrev_b32_e32 v10, 16, v10
	v_mul_f32_e32 v10, 0x3db504f3, v10
	v_mul_f32_e32 v10, v12, v10
	v_cvt_pk_bf16_f32 v10, v10, s0
	ds_write_b16 v110, v10
	v_exp_f32_e64 v10, -v6
	v_sub_f32_e32 v6, v7, v6
	v_exp_f32_e32 v6, v6
	s_waitcnt lgkmcnt(1)
	v_lshlrev_b32_e32 v11, 16, v11
	v_mul_f32_e32 v10, v10, v11
	v_cvt_pk_bf16_f32 v10, v10, s0
	v_mul_f32_e32 v6, v6, v11
	v_cvt_pk_bf16_f32 v6, v6, s0
	ds_write_b16 v110, v10 offset:17408
	ds_write_b16 v83, v6 offset:34834
	ds_read_u16 v10, v111 offset:59392
	ds_read_u16 v11, v112
	v_add_f32_e32 v6, v33, v9
	v_exp_f32_e32 v12, v6
	s_waitcnt lgkmcnt(1)
	v_lshlrev_b32_e32 v10, 16, v10
	v_mul_f32_e32 v10, 0x3db504f3, v10
	v_mul_f32_e32 v10, v12, v10
	v_cvt_pk_bf16_f32 v10, v10, s0
	ds_write_b16 v113, v10
	v_exp_f32_e64 v10, -v6
	v_sub_f32_e32 v6, v7, v6
	v_exp_f32_e32 v6, v6
	s_waitcnt lgkmcnt(1)
	v_lshlrev_b32_e32 v11, 16, v11
	v_mul_f32_e32 v10, v10, v11
	v_cvt_pk_bf16_f32 v10, v10, s0
	v_mul_f32_e32 v6, v6, v11
	v_cvt_pk_bf16_f32 v6, v6, s0
	ds_write_b16 v113, v10 offset:17408
	ds_write_b16 v83, v6 offset:34836
	ds_read_u16 v10, v114 offset:59392
	ds_read_u16 v11, v115
	v_add_f32_e32 v6, v63, v9
	v_exp_f32_e32 v12, v6
	s_waitcnt lgkmcnt(1)
	v_lshlrev_b32_e32 v10, 16, v10
	v_mul_f32_e32 v10, 0x3db504f3, v10
	v_mul_f32_e32 v10, v12, v10
	v_cvt_pk_bf16_f32 v10, v10, s0
	ds_write_b16 v116, v10
	v_exp_f32_e64 v10, -v6
	v_sub_f32_e32 v6, v7, v6
	v_exp_f32_e32 v6, v6
	s_waitcnt lgkmcnt(1)
	v_lshlrev_b32_e32 v11, 16, v11
	v_mul_f32_e32 v10, v10, v11
	v_cvt_pk_bf16_f32 v10, v10, s0
	v_mul_f32_e32 v6, v6, v11
	v_cvt_pk_bf16_f32 v6, v6, s0
	ds_write_b16 v116, v10 offset:17408
	ds_write_b16 v83, v6 offset:34838
	ds_read_u16 v10, v117 offset:59392
	ds_read_u16 v11, v118
	v_add_f32_e32 v6, v64, v9
	v_exp_f32_e32 v12, v6
	s_waitcnt lgkmcnt(1)
	v_lshlrev_b32_e32 v10, 16, v10
	v_mul_f32_e32 v10, 0x3db504f3, v10
	v_mul_f32_e32 v10, v12, v10
	v_cvt_pk_bf16_f32 v10, v10, s0
	ds_write_b16 v119, v10
	v_exp_f32_e64 v10, -v6
	v_sub_f32_e32 v6, v7, v6
	v_exp_f32_e32 v6, v6
	s_waitcnt lgkmcnt(1)
	v_lshlrev_b32_e32 v11, 16, v11
	v_mul_f32_e32 v10, v10, v11
	v_cvt_pk_bf16_f32 v10, v10, s0
	v_mul_f32_e32 v6, v6, v11
	v_cvt_pk_bf16_f32 v6, v6, s0
	ds_write_b16 v119, v10 offset:17408
	ds_write_b16 v83, v6 offset:34840
	ds_read_u16 v10, v120 offset:59392
	ds_read_u16 v11, v121
	v_add_f32_e32 v6, v65, v9
	v_exp_f32_e32 v12, v6
	s_waitcnt lgkmcnt(1)
	v_lshlrev_b32_e32 v10, 16, v10
	v_mul_f32_e32 v10, 0x3db504f3, v10
	v_mul_f32_e32 v10, v12, v10
	v_cvt_pk_bf16_f32 v10, v10, s0
	ds_write_b16 v122, v10
	v_exp_f32_e64 v10, -v6
	v_sub_f32_e32 v6, v7, v6
	v_exp_f32_e32 v6, v6
	s_waitcnt lgkmcnt(1)
	v_lshlrev_b32_e32 v11, 16, v11
	v_mul_f32_e32 v10, v10, v11
	v_cvt_pk_bf16_f32 v10, v10, s0
	v_mul_f32_e32 v6, v6, v11
	v_cvt_pk_bf16_f32 v6, v6, s0
	ds_write_b16 v122, v10 offset:17408
	ds_write_b16 v83, v6 offset:34842
	ds_read_u16 v10, v123 offset:59392
	ds_read_u16 v11, v124
	v_add_f32_e32 v6, v66, v9
	v_exp_f32_e32 v12, v6
	s_waitcnt lgkmcnt(1)
	v_lshlrev_b32_e32 v10, 16, v10
	v_mul_f32_e32 v10, 0x3db504f3, v10
	v_mul_f32_e32 v10, v12, v10
	v_cvt_pk_bf16_f32 v10, v10, s0
	ds_write_b16 v125, v10
	v_exp_f32_e64 v10, -v6
	v_sub_f32_e32 v6, v7, v6
	v_exp_f32_e32 v6, v6
	s_waitcnt lgkmcnt(1)
	v_lshlrev_b32_e32 v11, 16, v11
	v_mul_f32_e32 v10, v10, v11
	v_cvt_pk_bf16_f32 v10, v10, s0
	v_mul_f32_e32 v6, v6, v11
	v_cvt_pk_bf16_f32 v6, v6, s0
	ds_write_b16 v125, v10 offset:17408
	ds_write_b16 v83, v6 offset:34844
	v_add_f32_e32 v6, v9, v8
	ds_read_u16 v8, v126 offset:59392
	ds_read_u16 v9, v127
	v_exp_f32_e32 v10, v6
	s_waitcnt lgkmcnt(1)
	v_lshlrev_b32_e32 v8, 16, v8
	v_mul_f32_e32 v8, 0x3db504f3, v8
	v_mul_f32_e32 v8, v10, v8
	v_cvt_pk_bf16_f32 v8, v8, s0
	ds_write_b16 v128, v8
	v_exp_f32_e64 v8, -v6
	v_sub_f32_e32 v6, v7, v6
	v_exp_f32_e32 v6, v6
	s_waitcnt lgkmcnt(1)
	v_lshlrev_b32_e32 v9, 16, v9
	v_mul_f32_e32 v8, v8, v9
	v_cvt_pk_bf16_f32 v8, v8, s0
	v_mul_f32_e32 v6, v6, v9
	v_cvt_pk_bf16_f32 v6, v6, s0
	ds_write_b16 v128, v8 offset:17408
	ds_write_b16 v83, v6 offset:34846
	s_mov_b64 s[14:15], exec
	v_readlane_b32 vcc_lo, v254, 60
	v_readlane_b32 vcc_hi, v254, 61
	s_and_b64 vcc, s[14:15], vcc
	s_xor_b64 s[14:15], vcc, s[14:15]
	s_mov_b64 exec, vcc
	s_ashr_i32 s11, s10, 31
	s_or_saveexec_b64 s[14:15], s[14:15]
	v_mov_b64_e32 v[64:65], s[10:11]
	s_xor_b64 exec, exec, s[14:15]
	s_cbranch_execz .LBB0_287
	v_exp_f32_e32 v8, v7
	s_ashr_i32 s11, s10, 31
	s_lshl_b64 vcc, s[10:11], 9
	v_lshl_add_u64 v[6:7], v[36:37], 0, vcc
	v_mov_b64_e32 v[64:65], s[10:11]
	global_store_dword v[6:7], v8, off
	s_branch .LBB0_287
